# RWKV chain loop rewritten by hand: two register sets with persistent zero halves, ring flag polled early, next chunk loaded in the MFMA wait states
# baseline (speedup 1.0000x reference)
; DI void rk_step(const RkOps& c, f32x4 (&sT)[4], bf16* yb, int dir, int b, int hh, int vb, int cc, int fr, int qd) {
;     const f32x4 zero4 = (f32x4){0.f, 0.f, 0.f, 0.f};
;     union { unsigned u[4]; bf16x8_t v; } s0, s1;
;     s0.u[0] = cvtpk(sT[0][0], sT[0][1]); s0.u[1] = cvtpk(sT[0][2], sT[0][3]); s0.u[2] = cvtpk(sT[1][0], sT[1][1]); s0.u[3] = cvtpk(sT[1][2], sT[1][3]);
;     s1.u[0] = cvtpk(sT[2][0], sT[2][1]); s1.u[1] = cvtpk(sT[2][2], sT[2][3]); s1.u[2] = cvtpk(sT[3][0], sT[3][1]); s1.u[3] = cvtpk(sT[3][2], sT[3][3]);
;     f32x4 ax = MFMA16(widen4(c.lak), widen4(c.vv), zero4); ax = MFMA16(c.ah[0], s0.v, ax); ax = MFMA16(c.ah[1], s1.v, ax);
;     f32x4 ay = MFMA16(s0.v, c.rh[0], zero4); ay = MFMA16(s1.v, c.rh[1], ay);
;     const f32x4 au = MFMA16(widen4(c.tm), widen4(pack4(ax)), zero4);
;     const bf16x8_t vu = __builtin_shufflevector(c.vv, pack4(au), 0, 1, 2, 3, 4, 5, 6, 7);
;     ay = MFMA16(vu, c.mm, ay);
; #pragma unroll
;     for (int kt = 0; kt < 4; ++kt) sT[kt] = MFMA16(c.kb[kt], vu, sT[kt] * c.ge[kt]);
;     const int sgn = dir ? -1 : 1; const int tok0 = b * SEQ + (dir ? SEQ - 1 - 16 * cc : 16 * cc);
;     { u32x2_t w; w.x = cvtpk(ay[0], ay[1]); w.y = cvtpk(ay[2], ay[3]); *(u32x2_t*)(yb + ((size_t)dir * NT + tok0 + sgn * fr) * RW + hh * 64 + 16 * vb + 4 * qd) = w; }
; }
; DI void rk_load_lds(RkOps& o, const LAS unsigned char* pkg, int vb, int lane, int qd) {
; #pragma unroll
;     for (int ks = 0; ks < 2; ++ks) { o.ah[ks] = *(const LAS bf16x8_t*)(pkg + PK_AH + ks * 1024 + lane * 16); o.rh[ks] = *(const LAS bf16x8_t*)(pkg + PK_RH + ks * 1024 + lane * 16); }
; #pragma unroll
;     for (int kt = 0; kt < 4; ++kt) { o.kb[kt] = *(const LAS bf16x8_t*)(pkg + PK_KB + kt * 1024 + lane * 16); o.ge[kt] = *(const LAS f32x4*)(pkg + PK_GE + (16 * kt + 4 * qd) * 4); }
;     o.mm = *(const LAS bf16x8_t*)(pkg + PK_MM + lane * 16);
;     o.vv = *(const LAS bf16x4_t*)(pkg + PK_VV + vb * 512 + lane * 8); o.tm = *(const LAS bf16x4_t*)(pkg + PK_TM + lane * 8); o.lak = *(const LAS bf16x4_t*)(pkg + PK_LAK + lane * 8);
; }
; DI void rwkv_r2_unit(const Args& A, LAS unsigned char* lds, int u, int tid, int wave, int lane) {
;     ...
;         const int vb = wave; f32x4 sT[4];
; #pragma unroll
;         for (int kt = 0; kt < 4; ++kt) sT[kt] = (f32x4){0.f, 0.f, 0.f, 0.f};
;     ...
;         RkOps pa, pb;
;         RK_WAIT(0); rk_load_lds(pa, lds, vb, lane, qd);
.LBB0_654:
	s_add_i32 s10, s30, 47
	s_cmpk_lt_u32 s10, 0x5f
	s_cselect_b64 s[10:11], -1, 0
	s_cselect_b32 s39, 0, 0x7ff
	s_cselect_b32 s41, 16, 0xfffffff0
	s_ashr_i32 s15, s14, 31
	s_nop 1
	v_cndmask_b32_e64 v2, v158, v1, s[10:11]
	s_lshl_b64 s[16:17], s[14:15], 14
	v_ashrrev_i32_e32 v3, 31, v2
	v_lshl_add_u64 v[144:145], s[16:17], 0, v[2:3]
	s_lshl_b32 s16, s33, 6
	s_ashr_i32 s17, s16, 31
	s_lshl_b32 s42, s31, 11
	v_lshl_add_u64 v[154:155], s[16:17], 1, v[142:143]
	s_movk_i32 s40, 0x300
	s_mov_b32 s15, 0
	v_mov_b32_e32 v172, 0
	v_mov_b32_e32 v173, 0
	v_mov_b32_e32 v174, 0
	v_mov_b32_e32 v175, 0
	v_mov_b32_e32 v176, 0
	v_mov_b32_e32 v177, 0
	v_mov_b32_e32 v178, 0
	v_mov_b32_e32 v179, 0
	v_mov_b32_e32 v180, 0
	v_mov_b32_e32 v181, 0
	v_mov_b32_e32 v182, 0
	v_mov_b32_e32 v183, 0
	v_mov_b32_e32 v184, 0
	v_mov_b32_e32 v185, 0
	v_mov_b32_e32 v186, 0
	v_mov_b32_e32 v187, 0
	v_mov_b32_e32 v60, 0
	v_mov_b32_e32 v61, 0
	v_mov_b32_e32 v64, 0
	v_mov_b32_e32 v65, 0
	v_mov_b32_e32 v68, 0
	v_mov_b32_e32 v69, 0
	v_mov_b32_e32 v128, 0
	v_mov_b32_e32 v129, 0
	v_mov_b32_e32 v132, 0
	v_mov_b32_e32 v133, 0
	v_mov_b32_e32 v136, 0
	v_mov_b32_e32 v137, 0
	v_mov_b32_e32 v202, 0
	v_mov_b32_e32 v203, 0
	s_waitcnt vmcnt(0)
	s_mov_b32 s18, 0
	v_add_u32_e32 v216, s18, v148
	v_add_u32_e32 v217, s18, v157
	v_add_u32_e32 v218, s18, v150
	s_add_i32 s19, s18, s20
	v_add_u32_e32 v219, s19, v150
	ds_read_b64 v[58:59], v218 offset:11776
	ds_read_b64 v[62:63], v219 offset:8192
	ds_read_b128 v[6:9], v216
	ds_read_b128 v[10:13], v216 offset:1024
	ds_read_b128 v[14:17], v216 offset:2048
	ds_read_b128 v[18:21], v216 offset:3072
	ds_read_b128 v[42:45], v217 offset:12288
	ds_read_b128 v[46:49], v217 offset:12352
	ds_read_b128 v[50:53], v217 offset:12416
	ds_read_b128 v[54:57], v217 offset:12480
	ds_read_b64 v[66:67], v218 offset:10240
	ds_read_b64 v[70:71], v219 offset:8192
	ds_read_b128 v[38:41], v216 offset:10752
	ds_read_b128 v[22:25], v216 offset:4096
	ds_read_b128 v[26:29], v216 offset:5120
	ds_read_b128 v[30:33], v216 offset:6144
	ds_read_b128 v[34:37], v216 offset:7168
	s_waitcnt lgkmcnt(0)
.Lr20_loop:
	s_add_i32 s16, s15, 1
	s_cmpk_lt_u32 s16, 0x80
	s_cselect_b64 s[44:45], -1, 0
	s_and_b32 s17, s16, 7
	s_lshl_b32 s18, s17, 2
	s_add_i32 s18, s18, 0x18800
	s_add_i32 s46, s16, 1
	s_mulk_i32 s17, 0x3100
	v_mov_b32_e32 v212, s18
	ds_read_b32 v213, v212
	v_mfma_f32_16x16x32_bf16 v[196:199], v[58:61], v[62:65], 0
	v_cvt_pk_bf16_f32 v188, v172, v173
	v_cvt_pk_bf16_f32 v189, v174, v175
	v_cvt_pk_bf16_f32 v190, v176, v177
	v_cvt_pk_bf16_f32 v191, v178, v179
	v_cvt_pk_bf16_f32 v192, v180, v181
	v_cvt_pk_bf16_f32 v193, v182, v183
	v_mfma_f32_16x16x32_bf16 v[196:199], v[6:9], v[188:191], v[196:199]
	v_cvt_pk_bf16_f32 v194, v184, v185
	v_cvt_pk_bf16_f32 v195, v186, v187
	v_pk_mul_f32 v[172:173], v[172:173], v[42:43]
	v_pk_mul_f32 v[174:175], v[174:175], v[44:45]
	v_mfma_f32_16x16x32_bf16 v[196:199], v[10:13], v[192:195], v[196:199]
	v_mfma_f32_16x16x32_bf16 v[208:211], v[188:191], v[14:17], 0
	v_pk_mul_f32 v[176:177], v[176:177], v[46:47]
	v_pk_mul_f32 v[178:179], v[178:179], v[48:49]
	v_pk_mul_f32 v[180:181], v[180:181], v[50:51]
	v_pk_mul_f32 v[182:183], v[182:183], v[52:53]
	v_pk_mul_f32 v[184:185], v[184:185], v[54:55]
	v_pk_mul_f32 v[186:187], v[186:187], v[56:57]
	v_mfma_f32_16x16x32_bf16 v[208:211], v[192:195], v[18:21], v[208:211]
	s_or_b32 s16, s39, s42
	s_ashr_i32 s17, s16, 31
	v_lshl_add_u64 v[220:221], v[144:145], 0, s[16:17]
	s_add_i32 s39, s39, s41
	s_nop 1
	v_cvt_pk_bf16_f32 v200, v196, v197
	v_cvt_pk_bf16_f32 v201, v198, v199
	v_mad_u64_u32 v[222:223], s[16:17], v220, s40, v[154:155]
	v_mad_i32_i24 v223, v221, s40, v223
	v_mfma_f32_16x16x32_bf16 v[204:207], v[66:69], v[200:203], 0
	s_and_b64 vcc, exec, s[44:45]
	s_cbranch_vccz .Lr20_a_pad
	s_waitcnt lgkmcnt(0)
	v_cmp_eq_u32_e32 vcc, s46, v213
	s_cbranch_vccnz .Lr20_a_ready
	s_mov_b32 s47, 0x400000
; DI unsigned cvtpk(float lo, float hi) { const f2_t v = {lo, hi}; return __builtin_bit_cast(unsigned, __builtin_convertvector(v, bf2_t)); }
; DI void rk_step(const RkOps& c, f32x4 (&sT)[4], bf16* yb, int dir, int b, int hh, int vb, int cc, int fr, int qd) {
;     const f32x4 zero4 = (f32x4){0.f, 0.f, 0.f, 0.f};
;     union { unsigned u[4]; bf16x8_t v; } s0, s1;
;     s0.u[0] = cvtpk(sT[0][0], sT[0][1]); s0.u[1] = cvtpk(sT[0][2], sT[0][3]); s0.u[2] = cvtpk(sT[1][0], sT[1][1]); s0.u[3] = cvtpk(sT[1][2], sT[1][3]);
;     s1.u[0] = cvtpk(sT[2][0], sT[2][1]); s1.u[1] = cvtpk(sT[2][2], sT[2][3]); s1.u[2] = cvtpk(sT[3][0], sT[3][1]); s1.u[3] = cvtpk(sT[3][2], sT[3][3]);
;     f32x4 ax = MFMA16(widen4(c.lak), widen4(c.vv), zero4); ax = MFMA16(c.ah[0], s0.v, ax); ax = MFMA16(c.ah[1], s1.v, ax);
;     f32x4 ay = MFMA16(s0.v, c.rh[0], zero4); ay = MFMA16(s1.v, c.rh[1], ay);
;     const f32x4 au = MFMA16(widen4(c.tm), widen4(pack4(ax)), zero4);
;     const bf16x8_t vu = __builtin_shufflevector(c.vv, pack4(au), 0, 1, 2, 3, 4, 5, 6, 7);
;     ay = MFMA16(vu, c.mm, ay);
; #pragma unroll
;     for (int kt = 0; kt < 4; ++kt) sT[kt] = MFMA16(c.kb[kt], vu, sT[kt] * c.ge[kt]);
;     const int sgn = dir ? -1 : 1; const int tok0 = b * SEQ + (dir ? SEQ - 1 - 16 * cc : 16 * cc);
;     { u32x2_t w; w.x = cvtpk(ay[0], ay[1]); w.y = cvtpk(ay[2], ay[3]); *(u32x2_t*)(yb + ((size_t)dir * NT + tok0 + sgn * fr) * RW + hh * 64 + 16 * vb + 4 * qd) = w; }
; DI void rwkv_r2_unit(const Args& A, LAS unsigned char* lds, int u, int tid, int wave, int lane) {
;     ...
;         RkOps pa, pb;
;         RK_WAIT(0); rk_load_lds(pa, lds, vb, lane, qd);
;         for (int cc = 0; cc < 128; cc += 2) {
;             RK_WAIT(cc + 1); rk_load_lds(pb, lds + ((cc + 1) & (R2_SLOTS - 1)) * PKG_BYTES, vb, lane, qd);
;             rk_step(pa, sT, yb, dir, b, hh, vb, cc, fr, qd);
;             asm volatile("s_waitcnt lgkmcnt(0)" ::: "memory"); if (lane == 0) consumed[vb] = (unsigned)(cc + 2); asm volatile("" ::: "memory");
;             if (cc + 2 < 128) { RK_WAIT(cc + 2); rk_load_lds(pa, lds + ((cc + 2) & (R2_SLOTS - 1)) * PKG_BYTES, vb, lane, qd); }
;             rk_step(pb, sT, yb, dir, b, hh, vb, cc + 1, fr, qd);
;             if (cc + 2 < 128) { asm volatile("s_waitcnt lgkmcnt(0)" ::: "memory"); if (lane == 0) consumed[vb] = (unsigned)(cc + 3); asm volatile("" ::: "memory"); }
.Lr20_a_spin:
	s_sleep 1
	ds_read_b32 v213, v212
	s_add_i32 s47, s47, -1
	s_cmp_eq_u32 s47, 0
	s_cbranch_scc1 .Lr20_a_ready
	s_waitcnt lgkmcnt(0)
	v_cmp_eq_u32_e32 vcc, s46, v213
	s_cbranch_vccz .Lr20_a_spin
.Lr20_a_ready:
	s_add_i32 s17, s46, -1
	s_and_b32 s17, s17, 7
	s_mulk_i32 s17, 0x3100
	v_add_u32_e32 v216, s17, v148
	v_add_u32_e32 v217, s17, v157
	v_add_u32_e32 v218, s17, v150
	s_add_i32 s19, s17, s20
	v_add_u32_e32 v219, s19, v150
	ds_read_b64 v[126:127], v218 offset:11776
	ds_read_b64 v[130:131], v219 offset:8192
	ds_read_b128 v[74:77], v216
	ds_read_b128 v[78:81], v216 offset:1024
	ds_read_b128 v[82:85], v216 offset:2048
	ds_read_b128 v[86:89], v216 offset:3072
	ds_read_b128 v[110:113], v217 offset:12288
	ds_read_b128 v[114:117], v217 offset:12352
	ds_read_b128 v[118:121], v217 offset:12416
	ds_read_b128 v[122:125], v217 offset:12480
	ds_read_b64 v[134:135], v218 offset:10240
	ds_read_b64 v[138:139], v219 offset:8192
	ds_read_b128 v[106:109], v216 offset:10752
	ds_read_b128 v[90:93], v216 offset:4096
	ds_read_b128 v[94:97], v216 offset:5120
	ds_read_b128 v[98:101], v216 offset:6144
	ds_read_b128 v[102:105], v216 offset:7168
.Lr20_a_noload:
	v_cvt_pk_bf16_f32 v72, v204, v205
	v_cvt_pk_bf16_f32 v73, v206, v207
	s_nop 1
	v_mfma_f32_16x16x32_bf16 v[208:211], v[70:73], v[38:41], v[208:211]
	v_mfma_f32_16x16x32_bf16 v[172:175], v[22:25], v[70:73], v[172:175]
	v_mfma_f32_16x16x32_bf16 v[176:179], v[26:29], v[70:73], v[176:179]
	v_mfma_f32_16x16x32_bf16 v[180:183], v[30:33], v[70:73], v[180:183]
	v_mfma_f32_16x16x32_bf16 v[184:187], v[34:37], v[70:73], v[184:187]
	s_nop 3
	v_cvt_pk_bf16_f32 v224, v208, v209
	v_cvt_pk_bf16_f32 v225, v210, v211
	global_store_dwordx2 v[222:223], v[224:225], off
	s_and_b64 vcc, exec, s[44:45]
	s_cbranch_vccz .Lr20_a_norel
	s_waitcnt lgkmcnt(0)
	s_and_saveexec_b64 s[16:17], s[4:5]
	v_mov_b32_e32 v214, s21
	v_mov_b32_e32 v215, s46
	ds_write_b32 v214, v215
	s_or_b64 exec, exec, s[16:17]
.Lr20_a_norel:
	s_add_i32 s16, s15, 2
	s_cmpk_lt_u32 s16, 0x80
	s_cselect_b64 s[44:45], -1, 0
	s_and_b32 s17, s16, 7
	s_lshl_b32 s18, s17, 2
	s_add_i32 s18, s18, 0x18800
	s_add_i32 s46, s16, 1
	s_mulk_i32 s17, 0x3100
	v_mov_b32_e32 v212, s18
	ds_read_b32 v213, v212
	v_mfma_f32_16x16x32_bf16 v[196:199], v[126:129], v[130:133], 0
	v_cvt_pk_bf16_f32 v188, v172, v173
	v_cvt_pk_bf16_f32 v189, v174, v175
	v_cvt_pk_bf16_f32 v190, v176, v177
	v_cvt_pk_bf16_f32 v191, v178, v179
	v_cvt_pk_bf16_f32 v192, v180, v181
	v_cvt_pk_bf16_f32 v193, v182, v183
	v_mfma_f32_16x16x32_bf16 v[196:199], v[74:77], v[188:191], v[196:199]
	v_cvt_pk_bf16_f32 v194, v184, v185
	v_cvt_pk_bf16_f32 v195, v186, v187
	v_pk_mul_f32 v[172:173], v[172:173], v[110:111]
	v_pk_mul_f32 v[174:175], v[174:175], v[112:113]
	v_mfma_f32_16x16x32_bf16 v[196:199], v[78:81], v[192:195], v[196:199]
	v_mfma_f32_16x16x32_bf16 v[208:211], v[188:191], v[82:85], 0
	v_pk_mul_f32 v[176:177], v[176:177], v[114:115]
	v_pk_mul_f32 v[178:179], v[178:179], v[116:117]
	v_pk_mul_f32 v[180:181], v[180:181], v[118:119]
	v_pk_mul_f32 v[182:183], v[182:183], v[120:121]
	v_pk_mul_f32 v[184:185], v[184:185], v[122:123]
	v_pk_mul_f32 v[186:187], v[186:187], v[124:125]
	v_mfma_f32_16x16x32_bf16 v[208:211], v[192:195], v[86:89], v[208:211]
	s_or_b32 s16, s39, s42
	s_ashr_i32 s17, s16, 31
	v_lshl_add_u64 v[220:221], v[144:145], 0, s[16:17]
	s_add_i32 s39, s39, s41
	s_nop 1
	v_cvt_pk_bf16_f32 v200, v196, v197
	v_cvt_pk_bf16_f32 v201, v198, v199
	v_mad_u64_u32 v[222:223], s[16:17], v220, s40, v[154:155]
	v_mad_i32_i24 v223, v221, s40, v223
	v_mfma_f32_16x16x32_bf16 v[204:207], v[134:137], v[200:203], 0
	s_and_b64 vcc, exec, s[44:45]
	s_cbranch_vccz .Lr20_b_pad
	s_waitcnt lgkmcnt(0)
	v_cmp_eq_u32_e32 vcc, s46, v213
	s_cbranch_vccnz .Lr20_b_ready
	s_mov_b32 s47, 0x400000

; DI unsigned cvtpk(float lo, float hi) { const f2_t v = {lo, hi}; return __builtin_bit_cast(unsigned, __builtin_convertvector(v, bf2_t)); }
; DI void rk_step(const RkOps& c, f32x4 (&sT)[4], bf16* yb, int dir, int b, int hh, int vb, int cc, int fr, int qd) {
;     const f32x4 zero4 = (f32x4){0.f, 0.f, 0.f, 0.f};
;     union { unsigned u[4]; bf16x8_t v; } s0, s1;
;     s0.u[0] = cvtpk(sT[0][0], sT[0][1]); s0.u[1] = cvtpk(sT[0][2], sT[0][3]); s0.u[2] = cvtpk(sT[1][0], sT[1][1]); s0.u[3] = cvtpk(sT[1][2], sT[1][3]);
;     s1.u[0] = cvtpk(sT[2][0], sT[2][1]); s1.u[1] = cvtpk(sT[2][2], sT[2][3]); s1.u[2] = cvtpk(sT[3][0], sT[3][1]); s1.u[3] = cvtpk(sT[3][2], sT[3][3]);
;     f32x4 ax = MFMA16(widen4(c.lak), widen4(c.vv), zero4); ax = MFMA16(c.ah[0], s0.v, ax); ax = MFMA16(c.ah[1], s1.v, ax);
;     f32x4 ay = MFMA16(s0.v, c.rh[0], zero4); ay = MFMA16(s1.v, c.rh[1], ay);
;     const f32x4 au = MFMA16(widen4(c.tm), widen4(pack4(ax)), zero4);
;     const bf16x8_t vu = __builtin_shufflevector(c.vv, pack4(au), 0, 1, 2, 3, 4, 5, 6, 7);
;     ay = MFMA16(vu, c.mm, ay);
; #pragma unroll
;     for (int kt = 0; kt < 4; ++kt) sT[kt] = MFMA16(c.kb[kt], vu, sT[kt] * c.ge[kt]);
;     const int sgn = dir ? -1 : 1; const int tok0 = b * SEQ + (dir ? SEQ - 1 - 16 * cc : 16 * cc);
;     { u32x2_t w; w.x = cvtpk(ay[0], ay[1]); w.y = cvtpk(ay[2], ay[3]); *(u32x2_t*)(yb + ((size_t)dir * NT + tok0 + sgn * fr) * RW + hh * 64 + 16 * vb + 4 * qd) = w; }
; DI void rwkv_r2_unit(const Args& A, LAS unsigned char* lds, int u, int tid, int wave, int lane) {
;     ...
;         RkOps pa, pb;
;         RK_WAIT(0); rk_load_lds(pa, lds, vb, lane, qd);
;         for (int cc = 0; cc < 128; cc += 2) {
;             RK_WAIT(cc + 1); rk_load_lds(pb, lds + ((cc + 1) & (R2_SLOTS - 1)) * PKG_BYTES, vb, lane, qd);
;             rk_step(pa, sT, yb, dir, b, hh, vb, cc, fr, qd);
;             asm volatile("s_waitcnt lgkmcnt(0)" ::: "memory"); if (lane == 0) consumed[vb] = (unsigned)(cc + 2); asm volatile("" ::: "memory");
;             if (cc + 2 < 128) { RK_WAIT(cc + 2); rk_load_lds(pa, lds + ((cc + 2) & (R2_SLOTS - 1)) * PKG_BYTES, vb, lane, qd); }
;             rk_step(pb, sT, yb, dir, b, hh, vb, cc + 1, fr, qd);
;             if (cc + 2 < 128) { asm volatile("s_waitcnt lgkmcnt(0)" ::: "memory"); if (lane == 0) consumed[vb] = (unsigned)(cc + 3); asm volatile("" ::: "memory"); }
.Lr20_b_ready:
	s_add_i32 s17, s46, -1
	s_and_b32 s17, s17, 7
	s_mulk_i32 s17, 0x3100
	v_add_u32_e32 v216, s17, v148
	v_add_u32_e32 v217, s17, v157
	v_add_u32_e32 v218, s17, v150
	s_add_i32 s19, s17, s20
	v_add_u32_e32 v219, s19, v150
	ds_read_b64 v[58:59], v218 offset:11776
	ds_read_b64 v[62:63], v219 offset:8192
	ds_read_b128 v[6:9], v216
	ds_read_b128 v[10:13], v216 offset:1024
	ds_read_b128 v[14:17], v216 offset:2048
	ds_read_b128 v[18:21], v216 offset:3072
	ds_read_b128 v[42:45], v217 offset:12288
	ds_read_b128 v[46:49], v217 offset:12352
	ds_read_b128 v[50:53], v217 offset:12416
	ds_read_b128 v[54:57], v217 offset:12480
	ds_read_b64 v[66:67], v218 offset:10240
	ds_read_b64 v[70:71], v219 offset:8192
	ds_read_b128 v[38:41], v216 offset:10752
	ds_read_b128 v[22:25], v216 offset:4096
	ds_read_b128 v[26:29], v216 offset:5120
	ds_read_b128 v[30:33], v216 offset:6144
	ds_read_b128 v[34:37], v216 offset:7168
.Lr20_b_noload:
	v_cvt_pk_bf16_f32 v140, v204, v205
	v_cvt_pk_bf16_f32 v141, v206, v207
	s_nop 1
	v_mfma_f32_16x16x32_bf16 v[208:211], v[138:141], v[106:109], v[208:211]
	v_mfma_f32_16x16x32_bf16 v[172:175], v[90:93], v[138:141], v[172:175]
	v_mfma_f32_16x16x32_bf16 v[176:179], v[94:97], v[138:141], v[176:179]
	v_mfma_f32_16x16x32_bf16 v[180:183], v[98:101], v[138:141], v[180:183]
	v_mfma_f32_16x16x32_bf16 v[184:187], v[102:105], v[138:141], v[184:187]
	s_nop 3
	v_cvt_pk_bf16_f32 v224, v208, v209
	v_cvt_pk_bf16_f32 v225, v210, v211
	global_store_dwordx2 v[222:223], v[224:225], off
	s_and_b64 vcc, exec, s[44:45]
	s_cbranch_vccz .Lr20_b_norel
	s_waitcnt lgkmcnt(0)
	s_and_saveexec_b64 s[16:17], s[4:5]
	v_mov_b32_e32 v214, s21
	v_mov_b32_e32 v215, s46
	ds_write_b32 v214, v215
	s_or_b64 exec, exec, s[16:17]
.Lr20_b_norel:
	s_add_i32 s15, s15, 2
	s_cmpk_lt_u32 s15, 0x80
	s_cbranch_scc1 .Lr20_loop
	s_branch .LBB0_680
.Lr20_a_pad:
	s_nop 7
	s_branch .Lr20_a_noload

; #define LAS __attribute__((address_space(3)))
; #define RK_WAIT(cc_) do { unsigned spins = 0; while (ready[(cc_) & (R2_SLOTS - 1)] != (unsigned)((cc_) + 1)) { if (++spins > (1u << 22)) break; __builtin_amdgcn_s_sleep(1); } asm volatile("" ::: "memory"); } while (0)
; DI void rk_load_lds(RkOps& o, const LAS unsigned char* pkg, int vb, int lane, int qd) {
; #pragma unroll
;     for (int ks = 0; ks < 2; ++ks) { o.ah[ks] = *(const LAS bf16x8_t*)(pkg + PK_AH + ks * 1024 + lane * 16); o.rh[ks] = *(const LAS bf16x8_t*)(pkg + PK_RH + ks * 1024 + lane * 16); }
; #pragma unroll
;     for (int kt = 0; kt < 4; ++kt) { o.kb[kt] = *(const LAS bf16x8_t*)(pkg + PK_KB + kt * 1024 + lane * 16); o.ge[kt] = *(const LAS f32x4*)(pkg + PK_GE + (16 * kt + 4 * qd) * 4); }
;     o.mm = *(const LAS bf16x8_t*)(pkg + PK_MM + lane * 16);
;     o.vv = *(const LAS bf16x4_t*)(pkg + PK_VV + vb * 512 + lane * 8); o.tm = *(const LAS bf16x4_t*)(pkg + PK_TM + lane * 8); o.lak = *(const LAS bf16x4_t*)(pkg + PK_LAK + lane * 8);
; }
; DI void rwkv_r2_unit(const Args& A, LAS unsigned char* lds, int u, int tid, int wave, int lane) {
;     ...
;         const int vb = wave; f32x4 sT[4];
; #pragma unroll
;         for (int kt = 0; kt < 4; ++kt) sT[kt] = (f32x4){0.f, 0.f, 0.f, 0.f};
;     ...
;         RkOps pa, pb;
;         RK_WAIT(0); rk_load_lds(pa, lds, vb, lane, qd);
.LBB0_2116:
	s_add_i32 s10, s35, 47
	s_cmpk_lt_u32 s10, 0x5f
	s_cselect_b64 s[10:11], -1, 0
	s_cselect_b32 s39, 0, 0x7ff
	s_cselect_b32 s41, 16, 0xfffffff0
	s_ashr_i32 s15, s14, 31
	s_nop 1
	v_cndmask_b32_e64 v2, v158, v1, s[10:11]
	s_lshl_b64 s[16:17], s[14:15], 14
	v_ashrrev_i32_e32 v3, 31, v2
	v_lshl_add_u64 v[144:145], s[16:17], 0, v[2:3]
	s_lshl_b32 s16, s37, 6
	s_ashr_i32 s17, s16, 31
	s_lshl_b32 s42, s36, 11
	v_lshl_add_u64 v[154:155], s[16:17], 1, v[142:143]
	s_movk_i32 s40, 0x300
	s_mov_b32 s15, 0
	v_mov_b32_e32 v172, 0
	v_mov_b32_e32 v173, 0
	v_mov_b32_e32 v174, 0
	v_mov_b32_e32 v175, 0
	v_mov_b32_e32 v176, 0
	v_mov_b32_e32 v177, 0
	v_mov_b32_e32 v178, 0
	v_mov_b32_e32 v179, 0
	v_mov_b32_e32 v180, 0
	v_mov_b32_e32 v181, 0
	v_mov_b32_e32 v182, 0
	v_mov_b32_e32 v183, 0
	v_mov_b32_e32 v184, 0
	v_mov_b32_e32 v185, 0
	v_mov_b32_e32 v186, 0
	v_mov_b32_e32 v187, 0
	v_mov_b32_e32 v60, 0
	v_mov_b32_e32 v61, 0
	v_mov_b32_e32 v64, 0
	v_mov_b32_e32 v65, 0
	v_mov_b32_e32 v68, 0
	v_mov_b32_e32 v69, 0
	v_mov_b32_e32 v128, 0
	v_mov_b32_e32 v129, 0
	v_mov_b32_e32 v132, 0
	v_mov_b32_e32 v133, 0
	v_mov_b32_e32 v136, 0
	v_mov_b32_e32 v137, 0
	v_mov_b32_e32 v202, 0
	v_mov_b32_e32 v203, 0
	s_waitcnt vmcnt(0)
	s_mov_b32 s18, 0
	v_add_u32_e32 v216, s18, v148
	v_add_u32_e32 v217, s18, v157
	v_add_u32_e32 v218, s18, v150
	s_add_i32 s19, s18, s20
	v_add_u32_e32 v219, s19, v150
	ds_read_b64 v[58:59], v218 offset:11776
	ds_read_b64 v[62:63], v219 offset:8192
	ds_read_b128 v[6:9], v216
	ds_read_b128 v[10:13], v216 offset:1024
	ds_read_b128 v[14:17], v216 offset:2048
	ds_read_b128 v[18:21], v216 offset:3072
	ds_read_b128 v[42:45], v217 offset:12288
	ds_read_b128 v[46:49], v217 offset:12352
	ds_read_b128 v[50:53], v217 offset:12416
	ds_read_b128 v[54:57], v217 offset:12480
	ds_read_b64 v[66:67], v218 offset:10240
	ds_read_b64 v[70:71], v219 offset:8192
	ds_read_b128 v[38:41], v216 offset:10752
	ds_read_b128 v[22:25], v216 offset:4096
	ds_read_b128 v[26:29], v216 offset:5120
	ds_read_b128 v[30:33], v216 offset:6144
	ds_read_b128 v[34:37], v216 offset:7168
	s_waitcnt lgkmcnt(0)
